# k-snake MFMA order in 4 GEMM K-loops: same-accumulator pairs back to back, k order alternating so every pair boundary shares an A or B fragment; MoBA QK chain as v085
# speedup vs baseline: 1.0082x; 1.0042x over previous
.LBB0_114:
	ds_read_b128 v[130:133], v220
	ds_read_b128 v[134:137], v220 offset:1024
	ds_read_b128 v[138:141], v220 offset:2048
	ds_read_b128 v[142:145], v220 offset:3072
	ds_read_b128 v[146:149], v221
	ds_read_b128 v[150:153], v221 offset:1024
	ds_read_b128 v[154:157], v221 offset:2048
	ds_read_b128 v[158:161], v221 offset:3072
	s_add_i32 s46, s64, 0xfff80080
	s_cmp_eq_u32 s84, 28
	s_cselect_b32 s87, s62, s46
	s_cselect_b32 s86, s63, s65
	s_or_b32 s85, s87, 0x80
	s_mov_b32 m0, s93
	ds_read_b128 v[162:165], v222
	ds_read_b128 v[166:169], v222 offset:1024
	ds_read_b128 v[170:173], v222 offset:2048
	ds_read_b128 v[174:177], v222 offset:3072
	ds_read_b128 v[178:181], v222 offset:4096
	ds_read_b128 v[182:185], v222 offset:5120
	ds_read_b128 v[186:189], v222 offset:6144
	ds_read_b128 v[212:215], v222 offset:7168
	buffer_load_dwordx4 v1, s[40:43], s64 offen lds
	s_mov_b32 m0, s94
	s_nop 0
	buffer_load_dwordx4 v216, s[40:43], s64 offen lds
	s_waitcnt vmcnt(8)
	s_waitcnt lgkmcnt(0)
	s_barrier
	s_waitcnt lgkmcnt(7)
	v_mfma_f32_16x16x32_bf16 v[126:129], v[130:133], v[162:165], v[126:129]
	v_mfma_f32_16x16x32_bf16 v[126:129], v[134:137], v[166:169], v[126:129]
	s_waitcnt lgkmcnt(5)
	v_mfma_f32_16x16x32_bf16 v[122:125], v[142:145], v[166:169], v[122:125]
	v_mfma_f32_16x16x32_bf16 v[122:125], v[138:141], v[162:165], v[122:125]
	s_waitcnt lgkmcnt(3)
	v_mfma_f32_16x16x32_bf16 v[106:109], v[138:141], v[170:173], v[106:109]
	v_mfma_f32_16x16x32_bf16 v[106:109], v[142:145], v[174:177], v[106:109]
	s_waitcnt lgkmcnt(1)
	v_mfma_f32_16x16x32_bf16 v[114:117], v[134:137], v[174:177], v[114:117]
	v_mfma_f32_16x16x32_bf16 v[114:117], v[130:133], v[170:173], v[114:117]
	v_mfma_f32_16x16x32_bf16 v[102:105], v[130:133], v[178:181], v[102:105]
	v_mfma_f32_16x16x32_bf16 v[102:105], v[134:137], v[182:185], v[102:105]
	v_mfma_f32_16x16x32_bf16 v[94:97], v[142:145], v[182:185], v[94:97]
	v_mfma_f32_16x16x32_bf16 v[94:97], v[138:141], v[178:181], v[94:97]
	v_mfma_f32_16x16x32_bf16 v[78:81], v[138:141], v[186:189], v[78:81]
	v_mfma_f32_16x16x32_bf16 v[78:81], v[142:145], v[212:215], v[78:81]
	s_waitcnt lgkmcnt(0)
	v_mfma_f32_16x16x32_bf16 v[86:89], v[134:137], v[212:215], v[86:89]
	v_mfma_f32_16x16x32_bf16 v[86:89], v[130:133], v[186:189], v[86:89]
	v_mfma_f32_16x16x32_bf16 v[118:121], v[146:149], v[162:165], v[118:121]
	v_mfma_f32_16x16x32_bf16 v[118:121], v[150:153], v[166:169], v[118:121]
	v_mfma_f32_16x16x32_bf16 v[110:113], v[158:161], v[166:169], v[110:113]
	v_mfma_f32_16x16x32_bf16 v[110:113], v[154:157], v[162:165], v[110:113]
	v_mfma_f32_16x16x32_bf16 v[90:93], v[154:157], v[170:173], v[90:93]
	v_mfma_f32_16x16x32_bf16 v[90:93], v[158:161], v[174:177], v[90:93]
	v_mfma_f32_16x16x32_bf16 v[98:101], v[150:153], v[174:177], v[98:101]
	v_mfma_f32_16x16x32_bf16 v[98:101], v[146:149], v[170:173], v[98:101]
	v_mfma_f32_16x16x32_bf16 v[82:85], v[146:149], v[178:181], v[82:85]
	v_mfma_f32_16x16x32_bf16 v[82:85], v[150:153], v[182:185], v[82:85]
	v_mfma_f32_16x16x32_bf16 v[74:77], v[158:161], v[182:185], v[74:77]
	v_mfma_f32_16x16x32_bf16 v[74:77], v[154:157], v[178:181], v[74:77]
	v_mfma_f32_16x16x32_bf16 v[66:69], v[154:157], v[186:189], v[66:69]
	v_mfma_f32_16x16x32_bf16 v[66:69], v[158:161], v[212:215], v[66:69]
	v_mfma_f32_16x16x32_bf16 v[70:73], v[150:153], v[212:215], v[70:73]
	v_mfma_f32_16x16x32_bf16 v[70:73], v[146:149], v[186:189], v[70:73]
	s_barrier
	s_mov_b32 m0, s69
	s_mov_b32 s46, s42
	s_mov_b32 s47, s43
	ds_read_b128 v[162:165], v222 offset:16384
	ds_read_b128 v[166:169], v222 offset:17408
	ds_read_b128 v[170:173], v222 offset:18432
	ds_read_b128 v[174:177], v222 offset:19456
	ds_read_b128 v[178:181], v222 offset:20480
	ds_read_b128 v[182:185], v222 offset:21504
	ds_read_b128 v[186:189], v222 offset:22528
	ds_read_b128 v[212:215], v222 offset:23552
	buffer_load_dwordx4 v191, s[44:47], s86 offen lds
	s_mov_b32 m0, s70
	s_add_i32 s88, s86, 0x80000
	buffer_load_dwordx4 v217, s[44:47], s86 offen lds
	s_mov_b32 m0, s71
	s_nop 0
	buffer_load_dwordx4 v191, s[44:47], s88 offen lds
	s_mov_b32 m0, s72
	s_nop 0
	buffer_load_dwordx4 v217, s[44:47], s88 offen lds
	s_mov_b32 m0, s68
	s_nop 0
	buffer_load_dwordx4 v1, s[40:43], s87 offen lds
	s_mov_b32 m0, s73
	s_nop 0
	buffer_load_dwordx4 v216, s[40:43], s87 offen lds
	s_waitcnt vmcnt(8)
	s_waitcnt lgkmcnt(0)
	s_barrier
	s_waitcnt lgkmcnt(7)
	v_mfma_f32_16x16x32_bf16 v[62:65], v[130:133], v[162:165], v[62:65]
	v_mfma_f32_16x16x32_bf16 v[62:65], v[134:137], v[166:169], v[62:65]
	s_waitcnt lgkmcnt(5)
	v_mfma_f32_16x16x32_bf16 v[58:61], v[142:145], v[166:169], v[58:61]
	v_mfma_f32_16x16x32_bf16 v[58:61], v[138:141], v[162:165], v[58:61]
	s_waitcnt lgkmcnt(3)
	v_mfma_f32_16x16x32_bf16 v[46:49], v[138:141], v[170:173], v[46:49]
	v_mfma_f32_16x16x32_bf16 v[46:49], v[142:145], v[174:177], v[46:49]
	s_waitcnt lgkmcnt(1)
	v_mfma_f32_16x16x32_bf16 v[54:57], v[134:137], v[174:177], v[54:57]
	v_mfma_f32_16x16x32_bf16 v[54:57], v[130:133], v[170:173], v[54:57]
	v_mfma_f32_16x16x32_bf16 v[38:41], v[130:133], v[178:181], v[38:41]
	v_mfma_f32_16x16x32_bf16 v[38:41], v[134:137], v[182:185], v[38:41]
	v_mfma_f32_16x16x32_bf16 v[30:33], v[142:145], v[182:185], v[30:33]
	v_mfma_f32_16x16x32_bf16 v[30:33], v[138:141], v[178:181], v[30:33]
	v_mfma_f32_16x16x32_bf16 v[14:17], v[138:141], v[186:189], v[14:17]
	v_mfma_f32_16x16x32_bf16 v[14:17], v[142:145], v[212:215], v[14:17]
	s_waitcnt lgkmcnt(0)
	v_mfma_f32_16x16x32_bf16 v[22:25], v[134:137], v[212:215], v[22:25]
	v_mfma_f32_16x16x32_bf16 v[22:25], v[130:133], v[186:189], v[22:25]
	v_mfma_f32_16x16x32_bf16 v[50:53], v[146:149], v[162:165], v[50:53]
	v_mfma_f32_16x16x32_bf16 v[50:53], v[150:153], v[166:169], v[50:53]
	v_mfma_f32_16x16x32_bf16 v[42:45], v[158:161], v[166:169], v[42:45]
	v_mfma_f32_16x16x32_bf16 v[42:45], v[154:157], v[162:165], v[42:45]
	v_mfma_f32_16x16x32_bf16 v[26:29], v[154:157], v[170:173], v[26:29]
	v_mfma_f32_16x16x32_bf16 v[26:29], v[158:161], v[174:177], v[26:29]
	v_mfma_f32_16x16x32_bf16 v[34:37], v[150:153], v[174:177], v[34:37]
	v_mfma_f32_16x16x32_bf16 v[34:37], v[146:149], v[170:173], v[34:37]
	v_mfma_f32_16x16x32_bf16 v[18:21], v[146:149], v[178:181], v[18:21]
	v_mfma_f32_16x16x32_bf16 v[18:21], v[150:153], v[182:185], v[18:21]
	v_mfma_f32_16x16x32_bf16 v[10:13], v[158:161], v[182:185], v[10:13]
	v_mfma_f32_16x16x32_bf16 v[10:13], v[154:157], v[178:181], v[10:13]
	v_mfma_f32_16x16x32_bf16 v[2:5], v[154:157], v[186:189], v[2:5]
	v_mfma_f32_16x16x32_bf16 v[2:5], v[158:161], v[212:215], v[2:5]
	v_mfma_f32_16x16x32_bf16 v[6:9], v[150:153], v[212:215], v[6:9]
	v_mfma_f32_16x16x32_bf16 v[6:9], v[146:149], v[186:189], v[6:9]
	s_barrier
	ds_read_b128 v[130:133], v223
	ds_read_b128 v[134:137], v223 offset:1024
	ds_read_b128 v[138:141], v223 offset:2048
	ds_read_b128 v[142:145], v223 offset:3072
	ds_read_b128 v[146:149], v224
	ds_read_b128 v[150:153], v224 offset:1024
	ds_read_b128 v[154:157], v224 offset:2048
	ds_read_b128 v[158:161], v224 offset:3072
	s_add_i32 s87, s87, 0x80000
	s_mov_b32 m0, s74
	ds_read_b128 v[162:165], v222 offset:32768
	ds_read_b128 v[166:169], v222 offset:33792
	ds_read_b128 v[170:173], v222 offset:34816
	ds_read_b128 v[174:177], v222 offset:35840
	ds_read_b128 v[178:181], v222 offset:36864
	ds_read_b128 v[182:185], v222 offset:37888
	ds_read_b128 v[186:189], v222 offset:38912
	ds_read_b128 v[212:215], v222 offset:39936
	buffer_load_dwordx4 v1, s[40:43], s87 offen lds
	s_mov_b32 m0, s75
	s_nop 0
	buffer_load_dwordx4 v216, s[40:43], s87 offen lds
	s_waitcnt vmcnt(8)
	s_waitcnt lgkmcnt(0)
	s_barrier
	s_waitcnt lgkmcnt(7)
	v_mfma_f32_16x16x32_bf16 v[126:129], v[130:133], v[162:165], v[126:129]
	v_mfma_f32_16x16x32_bf16 v[126:129], v[134:137], v[166:169], v[126:129]
	s_waitcnt lgkmcnt(5)
	v_mfma_f32_16x16x32_bf16 v[122:125], v[142:145], v[166:169], v[122:125]
	v_mfma_f32_16x16x32_bf16 v[122:125], v[138:141], v[162:165], v[122:125]
	s_waitcnt lgkmcnt(3)
	v_mfma_f32_16x16x32_bf16 v[106:109], v[138:141], v[170:173], v[106:109]
	v_mfma_f32_16x16x32_bf16 v[106:109], v[142:145], v[174:177], v[106:109]
	s_waitcnt lgkmcnt(1)
	v_mfma_f32_16x16x32_bf16 v[114:117], v[134:137], v[174:177], v[114:117]
	v_mfma_f32_16x16x32_bf16 v[114:117], v[130:133], v[170:173], v[114:117]
	v_mfma_f32_16x16x32_bf16 v[102:105], v[130:133], v[178:181], v[102:105]
	v_mfma_f32_16x16x32_bf16 v[102:105], v[134:137], v[182:185], v[102:105]
	v_mfma_f32_16x16x32_bf16 v[94:97], v[142:145], v[182:185], v[94:97]
	v_mfma_f32_16x16x32_bf16 v[94:97], v[138:141], v[178:181], v[94:97]
	v_mfma_f32_16x16x32_bf16 v[78:81], v[138:141], v[186:189], v[78:81]
	v_mfma_f32_16x16x32_bf16 v[78:81], v[142:145], v[212:215], v[78:81]
	s_waitcnt lgkmcnt(0)
	v_mfma_f32_16x16x32_bf16 v[86:89], v[134:137], v[212:215], v[86:89]
	v_mfma_f32_16x16x32_bf16 v[86:89], v[130:133], v[186:189], v[86:89]
	v_mfma_f32_16x16x32_bf16 v[118:121], v[146:149], v[162:165], v[118:121]
	v_mfma_f32_16x16x32_bf16 v[118:121], v[150:153], v[166:169], v[118:121]
	v_mfma_f32_16x16x32_bf16 v[110:113], v[158:161], v[166:169], v[110:113]
	v_mfma_f32_16x16x32_bf16 v[110:113], v[154:157], v[162:165], v[110:113]
	v_mfma_f32_16x16x32_bf16 v[90:93], v[154:157], v[170:173], v[90:93]
	v_mfma_f32_16x16x32_bf16 v[90:93], v[158:161], v[174:177], v[90:93]
	v_mfma_f32_16x16x32_bf16 v[98:101], v[150:153], v[174:177], v[98:101]
	v_mfma_f32_16x16x32_bf16 v[98:101], v[146:149], v[170:173], v[98:101]
	v_mfma_f32_16x16x32_bf16 v[82:85], v[146:149], v[178:181], v[82:85]
	v_mfma_f32_16x16x32_bf16 v[82:85], v[150:153], v[182:185], v[82:85]
	v_mfma_f32_16x16x32_bf16 v[74:77], v[158:161], v[182:185], v[74:77]
	v_mfma_f32_16x16x32_bf16 v[74:77], v[154:157], v[178:181], v[74:77]
	v_mfma_f32_16x16x32_bf16 v[66:69], v[154:157], v[186:189], v[66:69]
	v_mfma_f32_16x16x32_bf16 v[66:69], v[158:161], v[212:215], v[66:69]
	v_mfma_f32_16x16x32_bf16 v[70:73], v[150:153], v[212:215], v[70:73]
	v_mfma_f32_16x16x32_bf16 v[70:73], v[146:149], v[186:189], v[70:73]
	s_barrier
	s_mov_b32 m0, s79
	s_or_b32 s87, s86, 0x80
	ds_read_b128 v[162:165], v222 offset:49152
	ds_read_b128 v[166:169], v222 offset:50176
	ds_read_b128 v[170:173], v222 offset:51200
	ds_read_b128 v[174:177], v222 offset:52224
	ds_read_b128 v[178:181], v222 offset:53248
	ds_read_b128 v[182:185], v222 offset:54272
	ds_read_b128 v[186:189], v222 offset:55296
	ds_read_b128 v[212:215], v222 offset:56320
	buffer_load_dwordx4 v191, s[44:47], s87 offen lds
	s_mov_b32 m0, s80
	s_add_i32 s86, s86, 0x80080
	buffer_load_dwordx4 v217, s[44:47], s87 offen lds
	s_mov_b32 m0, s83
	s_nop 0
	buffer_load_dwordx4 v191, s[44:47], s86 offen lds
	s_mov_b32 m0, s92
	s_nop 0
	buffer_load_dwordx4 v217, s[44:47], s86 offen lds
	s_mov_b32 m0, s81
	s_nop 0
	buffer_load_dwordx4 v1, s[40:43], s85 offen lds
	s_mov_b32 m0, s82
	s_nop 0
	buffer_load_dwordx4 v216, s[40:43], s85 offen lds
	s_waitcnt vmcnt(8)
	s_waitcnt lgkmcnt(0)
	s_barrier
	s_waitcnt lgkmcnt(7)
	v_mfma_f32_16x16x32_bf16 v[62:65], v[130:133], v[162:165], v[62:65]
	v_mfma_f32_16x16x32_bf16 v[62:65], v[134:137], v[166:169], v[62:65]
	s_waitcnt lgkmcnt(5)
	v_mfma_f32_16x16x32_bf16 v[58:61], v[142:145], v[166:169], v[58:61]
	v_mfma_f32_16x16x32_bf16 v[58:61], v[138:141], v[162:165], v[58:61]
	s_waitcnt lgkmcnt(3)
	v_mfma_f32_16x16x32_bf16 v[46:49], v[138:141], v[170:173], v[46:49]
	v_mfma_f32_16x16x32_bf16 v[46:49], v[142:145], v[174:177], v[46:49]
	s_waitcnt lgkmcnt(1)
	v_mfma_f32_16x16x32_bf16 v[54:57], v[134:137], v[174:177], v[54:57]
	v_mfma_f32_16x16x32_bf16 v[54:57], v[130:133], v[170:173], v[54:57]
	v_mfma_f32_16x16x32_bf16 v[38:41], v[130:133], v[178:181], v[38:41]
	v_mfma_f32_16x16x32_bf16 v[38:41], v[134:137], v[182:185], v[38:41]
	v_mfma_f32_16x16x32_bf16 v[30:33], v[142:145], v[182:185], v[30:33]
	v_mfma_f32_16x16x32_bf16 v[30:33], v[138:141], v[178:181], v[30:33]
	v_mfma_f32_16x16x32_bf16 v[14:17], v[138:141], v[186:189], v[14:17]
	v_mfma_f32_16x16x32_bf16 v[14:17], v[142:145], v[212:215], v[14:17]
	s_waitcnt lgkmcnt(0)
	v_mfma_f32_16x16x32_bf16 v[22:25], v[134:137], v[212:215], v[22:25]
	v_mfma_f32_16x16x32_bf16 v[22:25], v[130:133], v[186:189], v[22:25]
	v_mfma_f32_16x16x32_bf16 v[50:53], v[146:149], v[162:165], v[50:53]
	v_mfma_f32_16x16x32_bf16 v[50:53], v[150:153], v[166:169], v[50:53]
	v_mfma_f32_16x16x32_bf16 v[42:45], v[158:161], v[166:169], v[42:45]
	v_mfma_f32_16x16x32_bf16 v[42:45], v[154:157], v[162:165], v[42:45]
	v_mfma_f32_16x16x32_bf16 v[26:29], v[154:157], v[170:173], v[26:29]
	v_mfma_f32_16x16x32_bf16 v[26:29], v[158:161], v[174:177], v[26:29]
	v_mfma_f32_16x16x32_bf16 v[34:37], v[150:153], v[174:177], v[34:37]
	v_mfma_f32_16x16x32_bf16 v[34:37], v[146:149], v[170:173], v[34:37]
	v_mfma_f32_16x16x32_bf16 v[18:21], v[146:149], v[178:181], v[18:21]
	v_mfma_f32_16x16x32_bf16 v[18:21], v[150:153], v[182:185], v[18:21]
	v_mfma_f32_16x16x32_bf16 v[10:13], v[158:161], v[182:185], v[10:13]
	v_mfma_f32_16x16x32_bf16 v[10:13], v[154:157], v[178:181], v[10:13]
	v_mfma_f32_16x16x32_bf16 v[2:5], v[154:157], v[186:189], v[2:5]
	v_mfma_f32_16x16x32_bf16 v[2:5], v[158:161], v[212:215], v[2:5]
	v_mfma_f32_16x16x32_bf16 v[6:9], v[150:153], v[212:215], v[6:9]
	v_mfma_f32_16x16x32_bf16 v[6:9], v[146:149], v[186:189], v[6:9]
	s_barrier
	s_add_i32 s84, s84, 2
	s_addk_i32 s64, 0x100
	s_addk_i32 s65, 0x100
	s_cmp_gt_u32 s84, 29
	s_cbranch_scc0 .LBB0_114
	s_and_b64 vcc, exec, s[56:57]
	s_cbranch_vccz .LBB0_127
	s_barrier
	s_cmp_gt_i32 s61, 23
	s_mov_b64 s[46:47], -1
	s_cbranch_scc1 .LBB0_128

.LBB0_686:
	v_add_u32_e32 v152, 0x10000, v138
	v_add_u32_e32 v168, 0x14000, v138
	ds_read_b128 v[140:143], v152
	ds_read_b128 v[144:147], v152 offset:1024
	ds_read_b128 v[148:151], v152 offset:2048
	ds_read_b128 v[152:155], v152 offset:3072
	ds_read_b128 v[156:159], v168
	ds_read_b128 v[160:163], v168 offset:1024
	ds_read_b128 v[164:167], v168 offset:2048
	ds_read_b128 v[168:171], v168 offset:3072
	s_add_i32 s10, s33, s52
	s_add_i32 s53, s27, s52
	s_add_i32 s11, s10, 0x1000
	s_addk_i32 s53, 0x1000
	s_cmp_eq_u32 s52, 0
	s_cselect_b32 s55, s49, s11
	s_cselect_b32 s54, s50, s53
	s_or_b32 s53, s55, 0x80
	s_add_i32 s10, s10, 0x80f80
	s_mov_b32 m0, s43
	ds_read_b128 v[172:175], v139
	ds_read_b128 v[176:179], v139 offset:1024
	ds_read_b128 v[180:183], v139 offset:2048
	ds_read_b128 v[184:187], v139 offset:3072
	ds_read_b128 v[188:191], v139 offset:4096
	ds_read_b128 v[192:195], v139 offset:5120
	ds_read_b128 v[196:199], v139 offset:6144
	ds_read_b128 v[200:203], v139 offset:7168
	buffer_load_dwordx4 v134, s[4:7], s10 offen lds
	s_mov_b32 m0, s44
	s_nop 0
	buffer_load_dwordx4 v136, s[4:7], s10 offen lds
	s_waitcnt vmcnt(8)
	s_waitcnt lgkmcnt(0)
	s_barrier
	s_waitcnt lgkmcnt(7)
	v_mfma_f32_16x16x32_bf16 v[126:129], v[140:143], v[172:175], v[126:129]
	v_mfma_f32_16x16x32_bf16 v[126:129], v[144:147], v[176:179], v[126:129]
	s_waitcnt lgkmcnt(5)
	v_mfma_f32_16x16x32_bf16 v[122:125], v[152:155], v[176:179], v[122:125]
	v_mfma_f32_16x16x32_bf16 v[122:125], v[148:151], v[172:175], v[122:125]
	s_waitcnt lgkmcnt(3)
	v_mfma_f32_16x16x32_bf16 v[106:109], v[148:151], v[180:183], v[106:109]
	v_mfma_f32_16x16x32_bf16 v[106:109], v[152:155], v[184:187], v[106:109]
	s_waitcnt lgkmcnt(1)
	v_mfma_f32_16x16x32_bf16 v[110:113], v[144:147], v[184:187], v[110:113]
	v_mfma_f32_16x16x32_bf16 v[110:113], v[140:143], v[180:183], v[110:113]
	v_mfma_f32_16x16x32_bf16 v[98:101], v[140:143], v[188:191], v[98:101]
	v_mfma_f32_16x16x32_bf16 v[98:101], v[144:147], v[192:195], v[98:101]
	v_mfma_f32_16x16x32_bf16 v[90:93], v[152:155], v[192:195], v[90:93]
	v_mfma_f32_16x16x32_bf16 v[90:93], v[148:151], v[188:191], v[90:93]
	v_mfma_f32_16x16x32_bf16 v[74:77], v[148:151], v[196:199], v[74:77]
	v_mfma_f32_16x16x32_bf16 v[74:77], v[152:155], v[200:203], v[74:77]
	s_waitcnt lgkmcnt(0)
	v_mfma_f32_16x16x32_bf16 v[82:85], v[144:147], v[200:203], v[82:85]
	v_mfma_f32_16x16x32_bf16 v[82:85], v[140:143], v[196:199], v[82:85]
	v_mfma_f32_16x16x32_bf16 v[118:121], v[156:159], v[172:175], v[118:121]
	v_mfma_f32_16x16x32_bf16 v[118:121], v[160:163], v[176:179], v[118:121]
	v_mfma_f32_16x16x32_bf16 v[114:117], v[168:171], v[176:179], v[114:117]
	v_mfma_f32_16x16x32_bf16 v[114:117], v[164:167], v[172:175], v[114:117]
	v_mfma_f32_16x16x32_bf16 v[94:97], v[164:167], v[180:183], v[94:97]
	v_mfma_f32_16x16x32_bf16 v[94:97], v[168:171], v[184:187], v[94:97]
	v_mfma_f32_16x16x32_bf16 v[102:105], v[160:163], v[184:187], v[102:105]
	v_mfma_f32_16x16x32_bf16 v[102:105], v[156:159], v[180:183], v[102:105]
	v_mfma_f32_16x16x32_bf16 v[86:89], v[156:159], v[188:191], v[86:89]
	v_mfma_f32_16x16x32_bf16 v[86:89], v[160:163], v[192:195], v[86:89]
	v_mfma_f32_16x16x32_bf16 v[78:81], v[168:171], v[192:195], v[78:81]
	v_mfma_f32_16x16x32_bf16 v[78:81], v[164:167], v[188:191], v[78:81]
	v_mfma_f32_16x16x32_bf16 v[66:69], v[164:167], v[196:199], v[66:69]
	v_mfma_f32_16x16x32_bf16 v[66:69], v[168:171], v[200:203], v[66:69]
	v_mfma_f32_16x16x32_bf16 v[70:73], v[160:163], v[200:203], v[70:73]
	v_mfma_f32_16x16x32_bf16 v[70:73], v[156:159], v[196:199], v[70:73]
	s_barrier
	s_mov_b32 m0, s26
	s_mov_b32 s10, s6
	s_mov_b32 s11, s7
	ds_read_b128 v[172:175], v139 offset:16384
	ds_read_b128 v[176:179], v139 offset:17408
	ds_read_b128 v[180:183], v139 offset:18432
	ds_read_b128 v[184:187], v139 offset:19456
	ds_read_b128 v[188:191], v139 offset:20480
	ds_read_b128 v[192:195], v139 offset:21504
	ds_read_b128 v[196:199], v139 offset:22528
	ds_read_b128 v[200:203], v139 offset:23552
	buffer_load_dwordx4 v135, s[8:11], s54 offen lds
	s_mov_b32 m0, s28
	s_add_i32 s56, s54, 0x80000
	buffer_load_dwordx4 v137, s[8:11], s54 offen lds
	s_mov_b32 m0, s29
	s_nop 0
	buffer_load_dwordx4 v135, s[8:11], s56 offen lds
	s_mov_b32 m0, s30
	s_nop 0
	buffer_load_dwordx4 v137, s[8:11], s56 offen lds
	s_mov_b32 m0, s25
	s_nop 0
	buffer_load_dwordx4 v134, s[4:7], s55 offen lds
	s_mov_b32 m0, s31
	s_nop 0
	buffer_load_dwordx4 v136, s[4:7], s55 offen lds
	s_waitcnt vmcnt(8)
	s_waitcnt lgkmcnt(0)
	s_barrier
	s_waitcnt lgkmcnt(7)
	v_mfma_f32_16x16x32_bf16 v[62:65], v[140:143], v[172:175], v[62:65]
	v_mfma_f32_16x16x32_bf16 v[62:65], v[144:147], v[176:179], v[62:65]
	s_waitcnt lgkmcnt(5)
	v_mfma_f32_16x16x32_bf16 v[58:61], v[152:155], v[176:179], v[58:61]
	v_mfma_f32_16x16x32_bf16 v[58:61], v[148:151], v[172:175], v[58:61]
	s_waitcnt lgkmcnt(3)
	v_mfma_f32_16x16x32_bf16 v[42:45], v[148:151], v[180:183], v[42:45]
	v_mfma_f32_16x16x32_bf16 v[42:45], v[152:155], v[184:187], v[42:45]
	s_waitcnt lgkmcnt(1)
	v_mfma_f32_16x16x32_bf16 v[46:49], v[144:147], v[184:187], v[46:49]
	v_mfma_f32_16x16x32_bf16 v[46:49], v[140:143], v[180:183], v[46:49]
	v_mfma_f32_16x16x32_bf16 v[30:33], v[140:143], v[188:191], v[30:33]
	v_mfma_f32_16x16x32_bf16 v[30:33], v[144:147], v[192:195], v[30:33]
	v_mfma_f32_16x16x32_bf16 v[26:29], v[152:155], v[192:195], v[26:29]
	v_mfma_f32_16x16x32_bf16 v[26:29], v[148:151], v[188:191], v[26:29]
	v_mfma_f32_16x16x32_bf16 v[10:13], v[148:151], v[196:199], v[10:13]
	v_mfma_f32_16x16x32_bf16 v[10:13], v[152:155], v[200:203], v[10:13]
	s_waitcnt lgkmcnt(0)
	v_mfma_f32_16x16x32_bf16 v[14:17], v[144:147], v[200:203], v[14:17]
	v_mfma_f32_16x16x32_bf16 v[14:17], v[140:143], v[196:199], v[14:17]
	v_mfma_f32_16x16x32_bf16 v[54:57], v[156:159], v[172:175], v[54:57]
	v_mfma_f32_16x16x32_bf16 v[54:57], v[160:163], v[176:179], v[54:57]
	v_mfma_f32_16x16x32_bf16 v[50:53], v[168:171], v[176:179], v[50:53]
	v_mfma_f32_16x16x32_bf16 v[50:53], v[164:167], v[172:175], v[50:53]
	v_mfma_f32_16x16x32_bf16 v[34:37], v[164:167], v[180:183], v[34:37]
	v_mfma_f32_16x16x32_bf16 v[34:37], v[168:171], v[184:187], v[34:37]
	v_mfma_f32_16x16x32_bf16 v[38:41], v[160:163], v[184:187], v[38:41]
	v_mfma_f32_16x16x32_bf16 v[38:41], v[156:159], v[180:183], v[38:41]
	v_mfma_f32_16x16x32_bf16 v[22:25], v[156:159], v[188:191], v[22:25]
	v_mfma_f32_16x16x32_bf16 v[22:25], v[160:163], v[192:195], v[22:25]
	v_mfma_f32_16x16x32_bf16 v[18:21], v[168:171], v[192:195], v[18:21]
	v_mfma_f32_16x16x32_bf16 v[18:21], v[164:167], v[188:191], v[18:21]
	v_mfma_f32_16x16x32_bf16 v[2:5], v[164:167], v[196:199], v[2:5]
	v_mfma_f32_16x16x32_bf16 v[2:5], v[168:171], v[200:203], v[2:5]
	v_mfma_f32_16x16x32_bf16 v[6:9], v[160:163], v[200:203], v[6:9]
	v_mfma_f32_16x16x32_bf16 v[6:9], v[156:159], v[196:199], v[6:9]
	s_barrier
	v_add_u32_e32 v152, 0x18000, v138
	v_add_u32_e32 v168, 0x1c000, v138
	ds_read_b128 v[140:143], v152
	ds_read_b128 v[144:147], v152 offset:1024
	ds_read_b128 v[148:151], v152 offset:2048
	ds_read_b128 v[152:155], v152 offset:3072
	ds_read_b128 v[156:159], v168
	ds_read_b128 v[160:163], v168 offset:1024
	ds_read_b128 v[164:167], v168 offset:2048
	ds_read_b128 v[168:171], v168 offset:3072
	s_add_i32 s55, s55, 0x80000
	s_mov_b32 m0, s34
	ds_read_b128 v[172:175], v139 offset:32768
	ds_read_b128 v[176:179], v139 offset:33792
	ds_read_b128 v[180:183], v139 offset:34816
	ds_read_b128 v[184:187], v139 offset:35840
	ds_read_b128 v[188:191], v139 offset:36864
	ds_read_b128 v[192:195], v139 offset:37888
	ds_read_b128 v[196:199], v139 offset:38912
	ds_read_b128 v[200:203], v139 offset:39936
	buffer_load_dwordx4 v134, s[4:7], s55 offen lds
	s_mov_b32 m0, s35
	s_nop 0
	buffer_load_dwordx4 v136, s[4:7], s55 offen lds
	s_waitcnt vmcnt(8)
	s_waitcnt lgkmcnt(0)
	s_barrier
	s_waitcnt lgkmcnt(7)
	v_mfma_f32_16x16x32_bf16 v[126:129], v[140:143], v[172:175], v[126:129]
	v_mfma_f32_16x16x32_bf16 v[126:129], v[144:147], v[176:179], v[126:129]
	s_waitcnt lgkmcnt(5)
	v_mfma_f32_16x16x32_bf16 v[122:125], v[152:155], v[176:179], v[122:125]
	v_mfma_f32_16x16x32_bf16 v[122:125], v[148:151], v[172:175], v[122:125]
	s_waitcnt lgkmcnt(3)
	v_mfma_f32_16x16x32_bf16 v[106:109], v[148:151], v[180:183], v[106:109]
	v_mfma_f32_16x16x32_bf16 v[106:109], v[152:155], v[184:187], v[106:109]
	s_waitcnt lgkmcnt(1)
	v_mfma_f32_16x16x32_bf16 v[110:113], v[144:147], v[184:187], v[110:113]
	v_mfma_f32_16x16x32_bf16 v[110:113], v[140:143], v[180:183], v[110:113]
	v_mfma_f32_16x16x32_bf16 v[98:101], v[140:143], v[188:191], v[98:101]
	v_mfma_f32_16x16x32_bf16 v[98:101], v[144:147], v[192:195], v[98:101]
	v_mfma_f32_16x16x32_bf16 v[90:93], v[152:155], v[192:195], v[90:93]
	v_mfma_f32_16x16x32_bf16 v[90:93], v[148:151], v[188:191], v[90:93]
	v_mfma_f32_16x16x32_bf16 v[74:77], v[148:151], v[196:199], v[74:77]
	v_mfma_f32_16x16x32_bf16 v[74:77], v[152:155], v[200:203], v[74:77]
	s_waitcnt lgkmcnt(0)
	v_mfma_f32_16x16x32_bf16 v[82:85], v[144:147], v[200:203], v[82:85]
	v_mfma_f32_16x16x32_bf16 v[82:85], v[140:143], v[196:199], v[82:85]
	v_mfma_f32_16x16x32_bf16 v[118:121], v[156:159], v[172:175], v[118:121]
	v_mfma_f32_16x16x32_bf16 v[118:121], v[160:163], v[176:179], v[118:121]
	v_mfma_f32_16x16x32_bf16 v[114:117], v[168:171], v[176:179], v[114:117]
	v_mfma_f32_16x16x32_bf16 v[114:117], v[164:167], v[172:175], v[114:117]
	v_mfma_f32_16x16x32_bf16 v[94:97], v[164:167], v[180:183], v[94:97]
	v_mfma_f32_16x16x32_bf16 v[94:97], v[168:171], v[184:187], v[94:97]
	v_mfma_f32_16x16x32_bf16 v[102:105], v[160:163], v[184:187], v[102:105]
	v_mfma_f32_16x16x32_bf16 v[102:105], v[156:159], v[180:183], v[102:105]
	v_mfma_f32_16x16x32_bf16 v[86:89], v[156:159], v[188:191], v[86:89]
	v_mfma_f32_16x16x32_bf16 v[86:89], v[160:163], v[192:195], v[86:89]
	v_mfma_f32_16x16x32_bf16 v[78:81], v[168:171], v[192:195], v[78:81]
	v_mfma_f32_16x16x32_bf16 v[78:81], v[164:167], v[188:191], v[78:81]
	v_mfma_f32_16x16x32_bf16 v[66:69], v[164:167], v[196:199], v[66:69]
	v_mfma_f32_16x16x32_bf16 v[66:69], v[168:171], v[200:203], v[66:69]
	v_mfma_f32_16x16x32_bf16 v[70:73], v[160:163], v[200:203], v[70:73]
	v_mfma_f32_16x16x32_bf16 v[70:73], v[156:159], v[196:199], v[70:73]
	s_barrier
	s_mov_b32 m0, s36
	s_or_b32 s55, s54, 0x80
	ds_read_b128 v[172:175], v139 offset:49152
	ds_read_b128 v[176:179], v139 offset:50176
	ds_read_b128 v[180:183], v139 offset:51200
	ds_read_b128 v[184:187], v139 offset:52224
	ds_read_b128 v[188:191], v139 offset:53248
	ds_read_b128 v[192:195], v139 offset:54272
	ds_read_b128 v[196:199], v139 offset:55296
	ds_read_b128 v[200:203], v139 offset:56320
	buffer_load_dwordx4 v135, s[8:11], s55 offen lds
	s_mov_b32 m0, s37
	s_add_i32 s54, s54, 0x80080
	buffer_load_dwordx4 v137, s[8:11], s55 offen lds
	s_mov_b32 m0, s41
	s_nop 0
	buffer_load_dwordx4 v135, s[8:11], s54 offen lds
	s_mov_b32 m0, s42
	s_nop 0
	buffer_load_dwordx4 v137, s[8:11], s54 offen lds
	s_mov_b32 m0, s38
	s_nop 0
	buffer_load_dwordx4 v134, s[4:7], s53 offen lds
	s_mov_b32 m0, s40
	s_nop 0
	buffer_load_dwordx4 v136, s[4:7], s53 offen lds
	s_waitcnt vmcnt(8)
	s_waitcnt lgkmcnt(0)
	s_barrier
	s_waitcnt lgkmcnt(7)
	v_mfma_f32_16x16x32_bf16 v[62:65], v[140:143], v[172:175], v[62:65]
	v_mfma_f32_16x16x32_bf16 v[62:65], v[144:147], v[176:179], v[62:65]
	s_waitcnt lgkmcnt(5)
	v_mfma_f32_16x16x32_bf16 v[58:61], v[152:155], v[176:179], v[58:61]
	v_mfma_f32_16x16x32_bf16 v[58:61], v[148:151], v[172:175], v[58:61]
	s_waitcnt lgkmcnt(3)
	v_mfma_f32_16x16x32_bf16 v[42:45], v[148:151], v[180:183], v[42:45]
	v_mfma_f32_16x16x32_bf16 v[42:45], v[152:155], v[184:187], v[42:45]
	s_waitcnt lgkmcnt(1)
	v_mfma_f32_16x16x32_bf16 v[46:49], v[144:147], v[184:187], v[46:49]
	v_mfma_f32_16x16x32_bf16 v[46:49], v[140:143], v[180:183], v[46:49]
	v_mfma_f32_16x16x32_bf16 v[30:33], v[140:143], v[188:191], v[30:33]
	v_mfma_f32_16x16x32_bf16 v[30:33], v[144:147], v[192:195], v[30:33]
	v_mfma_f32_16x16x32_bf16 v[26:29], v[152:155], v[192:195], v[26:29]
	v_mfma_f32_16x16x32_bf16 v[26:29], v[148:151], v[188:191], v[26:29]
	v_mfma_f32_16x16x32_bf16 v[10:13], v[148:151], v[196:199], v[10:13]
	v_mfma_f32_16x16x32_bf16 v[10:13], v[152:155], v[200:203], v[10:13]
	s_waitcnt lgkmcnt(0)
	v_mfma_f32_16x16x32_bf16 v[14:17], v[144:147], v[200:203], v[14:17]
	v_mfma_f32_16x16x32_bf16 v[14:17], v[140:143], v[196:199], v[14:17]
	v_mfma_f32_16x16x32_bf16 v[54:57], v[156:159], v[172:175], v[54:57]
	v_mfma_f32_16x16x32_bf16 v[54:57], v[160:163], v[176:179], v[54:57]
	v_mfma_f32_16x16x32_bf16 v[50:53], v[168:171], v[176:179], v[50:53]
	v_mfma_f32_16x16x32_bf16 v[50:53], v[164:167], v[172:175], v[50:53]
	v_mfma_f32_16x16x32_bf16 v[34:37], v[164:167], v[180:183], v[34:37]
	v_mfma_f32_16x16x32_bf16 v[34:37], v[168:171], v[184:187], v[34:37]
	v_mfma_f32_16x16x32_bf16 v[38:41], v[160:163], v[184:187], v[38:41]
	v_mfma_f32_16x16x32_bf16 v[38:41], v[156:159], v[180:183], v[38:41]
	v_mfma_f32_16x16x32_bf16 v[22:25], v[156:159], v[188:191], v[22:25]
	v_mfma_f32_16x16x32_bf16 v[22:25], v[160:163], v[192:195], v[22:25]
	v_mfma_f32_16x16x32_bf16 v[18:21], v[168:171], v[192:195], v[18:21]
	v_mfma_f32_16x16x32_bf16 v[18:21], v[164:167], v[188:191], v[18:21]
	v_mfma_f32_16x16x32_bf16 v[2:5], v[164:167], v[196:199], v[2:5]
	v_mfma_f32_16x16x32_bf16 v[2:5], v[168:171], v[200:203], v[2:5]
	v_mfma_f32_16x16x32_bf16 v[6:9], v[160:163], v[200:203], v[6:9]
	v_mfma_f32_16x16x32_bf16 v[6:9], v[156:159], v[196:199], v[6:9]
	s_barrier
	s_add_i32 s51, s51, 2
	s_addk_i32 s52, 0x100
	s_cmp_gt_u32 s51, 29
	s_cbranch_scc0 .LBB0_686
	s_andn2_b64 vcc, exec, s[2:3]
	s_cbranch_vccnz .LBB0_678
	v_mov_b32_e32 v2, 0
	s_mov_b32 s14, s46
	s_mov_b32 s15, s47
	s_mov_b32 s27, s48
	s_mov_b32 s33, s13
	s_mov_b32 s45, s12
	v_mov_b32_e32 v3, v2
	v_mov_b32_e32 v4, v2
	v_mov_b32_e32 v5, v2
	v_mov_b32_e32 v6, v2
	v_mov_b32_e32 v7, v2
	v_mov_b32_e32 v8, v2
	v_mov_b32_e32 v9, v2
	v_mov_b32_e32 v18, v2
	v_mov_b32_e32 v19, v2
	v_mov_b32_e32 v20, v2
	v_mov_b32_e32 v21, v2
	v_mov_b32_e32 v22, v2
	v_mov_b32_e32 v23, v2
	v_mov_b32_e32 v24, v2
	v_mov_b32_e32 v25, v2
	v_mov_b32_e32 v34, v2
	v_mov_b32_e32 v35, v2
	v_mov_b32_e32 v36, v2
	v_mov_b32_e32 v37, v2
	v_mov_b32_e32 v38, v2
	v_mov_b32_e32 v39, v2
	v_mov_b32_e32 v40, v2
	v_mov_b32_e32 v41, v2
	v_mov_b32_e32 v50, v2
	v_mov_b32_e32 v51, v2
	v_mov_b32_e32 v52, v2
	v_mov_b32_e32 v53, v2
	v_mov_b32_e32 v54, v2
	v_mov_b32_e32 v55, v2
	v_mov_b32_e32 v56, v2
	v_mov_b32_e32 v57, v2
	v_mov_b32_e32 v10, v2
	v_mov_b32_e32 v11, v2
	v_mov_b32_e32 v12, v2
	v_mov_b32_e32 v13, v2
	v_mov_b32_e32 v14, v2
	v_mov_b32_e32 v15, v2
	v_mov_b32_e32 v16, v2
	v_mov_b32_e32 v17, v2
	v_mov_b32_e32 v26, v2
	v_mov_b32_e32 v27, v2
	v_mov_b32_e32 v28, v2
	v_mov_b32_e32 v29, v2
	v_mov_b32_e32 v30, v2
	v_mov_b32_e32 v31, v2
	v_mov_b32_e32 v32, v2
	v_mov_b32_e32 v33, v2
	v_mov_b32_e32 v42, v2
	v_mov_b32_e32 v43, v2
	v_mov_b32_e32 v44, v2
	v_mov_b32_e32 v45, v2
	v_mov_b32_e32 v46, v2
	v_mov_b32_e32 v47, v2
	v_mov_b32_e32 v48, v2
	v_mov_b32_e32 v49, v2
	v_mov_b32_e32 v58, v2
	v_mov_b32_e32 v59, v2
	v_mov_b32_e32 v60, v2
	v_mov_b32_e32 v61, v2
	v_mov_b32_e32 v62, v2
	v_mov_b32_e32 v63, v2
	v_mov_b32_e32 v64, v2
	v_mov_b32_e32 v65, v2
	v_mov_b32_e32 v66, v2
	v_mov_b32_e32 v67, v2
	v_mov_b32_e32 v68, v2
	v_mov_b32_e32 v69, v2
	v_mov_b32_e32 v70, v2
	v_mov_b32_e32 v71, v2
	v_mov_b32_e32 v72, v2
	v_mov_b32_e32 v73, v2
	v_mov_b32_e32 v78, v2
	v_mov_b32_e32 v79, v2
	v_mov_b32_e32 v80, v2
	v_mov_b32_e32 v81, v2
	v_mov_b32_e32 v86, v2
	v_mov_b32_e32 v87, v2
	v_mov_b32_e32 v88, v2
	v_mov_b32_e32 v89, v2
	v_mov_b32_e32 v94, v2
	v_mov_b32_e32 v95, v2
	v_mov_b32_e32 v96, v2
	v_mov_b32_e32 v97, v2
	v_mov_b32_e32 v102, v2
	v_mov_b32_e32 v103, v2
	v_mov_b32_e32 v104, v2
	v_mov_b32_e32 v105, v2
	v_mov_b32_e32 v114, v2
	v_mov_b32_e32 v115, v2
	v_mov_b32_e32 v116, v2
	v_mov_b32_e32 v117, v2
	v_mov_b32_e32 v118, v2
	v_mov_b32_e32 v119, v2
	v_mov_b32_e32 v120, v2
	v_mov_b32_e32 v121, v2
	v_mov_b32_e32 v74, v2
	v_mov_b32_e32 v75, v2
	v_mov_b32_e32 v76, v2
	v_mov_b32_e32 v77, v2
	v_mov_b32_e32 v82, v2
	v_mov_b32_e32 v83, v2
	v_mov_b32_e32 v84, v2
	v_mov_b32_e32 v85, v2
	v_mov_b32_e32 v90, v2
	v_mov_b32_e32 v91, v2
	v_mov_b32_e32 v92, v2
	v_mov_b32_e32 v93, v2
	v_mov_b32_e32 v98, v2
	v_mov_b32_e32 v99, v2
	v_mov_b32_e32 v100, v2
	v_mov_b32_e32 v101, v2
	v_mov_b32_e32 v106, v2
	v_mov_b32_e32 v107, v2
	v_mov_b32_e32 v108, v2
	v_mov_b32_e32 v109, v2
	v_mov_b32_e32 v110, v2
	v_mov_b32_e32 v111, v2
	v_mov_b32_e32 v112, v2
	v_mov_b32_e32 v113, v2
	v_mov_b32_e32 v122, v2
	v_mov_b32_e32 v123, v2
	v_mov_b32_e32 v124, v2
	v_mov_b32_e32 v125, v2
	v_mov_b32_e32 v126, v2
	v_mov_b32_e32 v127, v2
	v_mov_b32_e32 v128, v2
	v_mov_b32_e32 v129, v2
	s_branch .LBB0_678

.LBB0_907:
	v_add_u32_e32 v166, 0x10000, v179
	ds_read_b128 v[162:165], v166
	ds_read_b128 v[182:185], v166 offset:1024
	ds_read_b128 v[186:189], v166 offset:2048
	ds_read_b128 v[190:193], v166 offset:3072
	v_add_u32_e32 v166, 0x14000, v179
	ds_read_b128 v[194:197], v166
	ds_read_b128 v[198:201], v166 offset:1024
	ds_read_b128 v[202:205], v166 offset:2048
	ds_read_b128 v[206:209], v166 offset:3072
	s_add_i32 s10, s45, s64
	s_add_i32 s26, s40, s64
	s_add_i32 s11, s10, 0x1000
	s_addk_i32 s26, 0x1000
	s_cmp_eq_u32 s64, 0
	s_cselect_b32 s29, s62, s11
	s_cselect_b32 s27, s63, s26
	s_add_i32 s26, s29, 0x80
	s_add_i32 s28, s27, 0x80
	s_add_i32 s10, s10, 0x80f80
	s_mov_b32 m0, s55
	ds_read_b128 v[210:213], v180
	ds_read_b128 v[214:217], v180 offset:1024
	ds_read_b128 v[218:221], v180 offset:2048
	ds_read_b128 v[222:225], v180 offset:3072
	ds_read_b128 v[226:229], v180 offset:4096
	ds_read_b128 v[230:233], v180 offset:5120
	ds_read_b128 v[234:237], v180 offset:6144
	ds_read_b128 v[238:241], v180 offset:7168
	buffer_load_dwordx4 v1, s[4:7], s10 offen lds
	s_mov_b32 m0, s56
	s_nop 0
	buffer_load_dwordx4 v175, s[4:7], s10 offen lds
	s_waitcnt vmcnt(8)
	s_waitcnt lgkmcnt(0)
	s_barrier
	s_waitcnt lgkmcnt(7)
	v_mfma_f32_16x16x32_bf16 v[126:129], v[162:165], v[210:213], v[126:129]
	v_mfma_f32_16x16x32_bf16 v[126:129], v[182:185], v[214:217], v[126:129]
	s_waitcnt lgkmcnt(5)
	v_mfma_f32_16x16x32_bf16 v[122:125], v[190:193], v[214:217], v[122:125]
	v_mfma_f32_16x16x32_bf16 v[122:125], v[186:189], v[210:213], v[122:125]
	s_waitcnt lgkmcnt(3)
	v_mfma_f32_16x16x32_bf16 v[114:117], v[186:189], v[218:221], v[114:117]
	v_mfma_f32_16x16x32_bf16 v[114:117], v[190:193], v[222:225], v[114:117]
	s_waitcnt lgkmcnt(1)
	v_mfma_f32_16x16x32_bf16 v[118:121], v[182:185], v[222:225], v[118:121]
	v_mfma_f32_16x16x32_bf16 v[118:121], v[162:165], v[218:221], v[118:121]
	v_mfma_f32_16x16x32_bf16 v[110:113], v[162:165], v[226:229], v[110:113]
	v_mfma_f32_16x16x32_bf16 v[110:113], v[182:185], v[230:233], v[110:113]
	v_mfma_f32_16x16x32_bf16 v[106:109], v[190:193], v[230:233], v[106:109]
	v_mfma_f32_16x16x32_bf16 v[106:109], v[186:189], v[226:229], v[106:109]
	v_mfma_f32_16x16x32_bf16 v[98:101], v[186:189], v[234:237], v[98:101]
	v_mfma_f32_16x16x32_bf16 v[98:101], v[190:193], v[238:241], v[98:101]
	s_waitcnt lgkmcnt(0)
	v_mfma_f32_16x16x32_bf16 v[102:105], v[182:185], v[238:241], v[102:105]
	v_mfma_f32_16x16x32_bf16 v[102:105], v[162:165], v[234:237], v[102:105]
	v_mfma_f32_16x16x32_bf16 v[94:97], v[194:197], v[210:213], v[94:97]
	v_mfma_f32_16x16x32_bf16 v[94:97], v[198:201], v[214:217], v[94:97]
	v_mfma_f32_16x16x32_bf16 v[90:93], v[206:209], v[214:217], v[90:93]
	v_mfma_f32_16x16x32_bf16 v[90:93], v[202:205], v[210:213], v[90:93]
	v_mfma_f32_16x16x32_bf16 v[82:85], v[202:205], v[218:221], v[82:85]
	v_mfma_f32_16x16x32_bf16 v[82:85], v[206:209], v[222:225], v[82:85]
	v_mfma_f32_16x16x32_bf16 v[86:89], v[198:201], v[222:225], v[86:89]
	v_mfma_f32_16x16x32_bf16 v[86:89], v[194:197], v[218:221], v[86:89]
	v_mfma_f32_16x16x32_bf16 v[78:81], v[194:197], v[226:229], v[78:81]
	v_mfma_f32_16x16x32_bf16 v[78:81], v[198:201], v[230:233], v[78:81]
	v_mfma_f32_16x16x32_bf16 v[74:77], v[206:209], v[230:233], v[74:77]
	v_mfma_f32_16x16x32_bf16 v[74:77], v[202:205], v[226:229], v[74:77]
	v_mfma_f32_16x16x32_bf16 v[66:69], v[202:205], v[234:237], v[66:69]
	v_mfma_f32_16x16x32_bf16 v[66:69], v[206:209], v[238:241], v[66:69]
	v_mfma_f32_16x16x32_bf16 v[70:73], v[198:201], v[238:241], v[70:73]
	v_mfma_f32_16x16x32_bf16 v[70:73], v[194:197], v[234:237], v[70:73]
	s_barrier
	s_mov_b32 m0, s37
	s_mov_b32 s10, s6
	s_mov_b32 s11, s7
	ds_read_b128 v[210:213], v180 offset:16384
	ds_read_b128 v[214:217], v180 offset:17408
	ds_read_b128 v[218:221], v180 offset:18432
	ds_read_b128 v[222:225], v180 offset:19456
	ds_read_b128 v[226:229], v180 offset:20480
	ds_read_b128 v[230:233], v180 offset:21504
	ds_read_b128 v[234:237], v180 offset:22528
	ds_read_b128 v[238:241], v180 offset:23552
	buffer_load_dwordx4 v174, s[8:11], s27 offen lds
	s_mov_b32 m0, s38
	s_add_i32 s66, s27, 0x80000
	buffer_load_dwordx4 v176, s[8:11], s27 offen lds
	s_mov_b32 m0, s39
	s_nop 0
	buffer_load_dwordx4 v174, s[8:11], s66 offen lds
	s_mov_b32 m0, s41
	s_nop 0
	buffer_load_dwordx4 v176, s[8:11], s66 offen lds
	s_mov_b32 m0, s36
	s_nop 0
	buffer_load_dwordx4 v1, s[4:7], s29 offen lds
	s_mov_b32 m0, s42
	s_nop 0
	buffer_load_dwordx4 v175, s[4:7], s29 offen lds
	s_waitcnt vmcnt(8)
	s_waitcnt lgkmcnt(0)
	s_barrier
	s_waitcnt lgkmcnt(7)
	v_mfma_f32_16x16x32_bf16 v[62:65], v[162:165], v[210:213], v[62:65]
	v_mfma_f32_16x16x32_bf16 v[62:65], v[182:185], v[214:217], v[62:65]
	s_waitcnt lgkmcnt(5)
	v_mfma_f32_16x16x32_bf16 v[58:61], v[190:193], v[214:217], v[58:61]
	v_mfma_f32_16x16x32_bf16 v[58:61], v[186:189], v[210:213], v[58:61]
	s_waitcnt lgkmcnt(3)
	v_mfma_f32_16x16x32_bf16 v[50:53], v[186:189], v[218:221], v[50:53]
	v_mfma_f32_16x16x32_bf16 v[50:53], v[190:193], v[222:225], v[50:53]
	s_waitcnt lgkmcnt(1)
	v_mfma_f32_16x16x32_bf16 v[54:57], v[182:185], v[222:225], v[54:57]
	v_mfma_f32_16x16x32_bf16 v[54:57], v[162:165], v[218:221], v[54:57]
	v_mfma_f32_16x16x32_bf16 v[46:49], v[162:165], v[226:229], v[46:49]
	v_mfma_f32_16x16x32_bf16 v[46:49], v[182:185], v[230:233], v[46:49]
	v_mfma_f32_16x16x32_bf16 v[42:45], v[190:193], v[230:233], v[42:45]
	v_mfma_f32_16x16x32_bf16 v[42:45], v[186:189], v[226:229], v[42:45]
	v_mfma_f32_16x16x32_bf16 v[34:37], v[186:189], v[234:237], v[34:37]
	v_mfma_f32_16x16x32_bf16 v[34:37], v[190:193], v[238:241], v[34:37]
	s_waitcnt lgkmcnt(0)
	v_mfma_f32_16x16x32_bf16 v[38:41], v[182:185], v[238:241], v[38:41]
	v_mfma_f32_16x16x32_bf16 v[38:41], v[162:165], v[234:237], v[38:41]
	v_mfma_f32_16x16x32_bf16 v[30:33], v[194:197], v[210:213], v[30:33]
	v_mfma_f32_16x16x32_bf16 v[30:33], v[198:201], v[214:217], v[30:33]
	v_mfma_f32_16x16x32_bf16 v[26:29], v[206:209], v[214:217], v[26:29]
	v_mfma_f32_16x16x32_bf16 v[26:29], v[202:205], v[210:213], v[26:29]
	v_mfma_f32_16x16x32_bf16 v[18:21], v[202:205], v[218:221], v[18:21]
	v_mfma_f32_16x16x32_bf16 v[18:21], v[206:209], v[222:225], v[18:21]
	v_mfma_f32_16x16x32_bf16 v[22:25], v[198:201], v[222:225], v[22:25]
	v_mfma_f32_16x16x32_bf16 v[22:25], v[194:197], v[218:221], v[22:25]
	v_mfma_f32_16x16x32_bf16 v[14:17], v[194:197], v[226:229], v[14:17]
	v_mfma_f32_16x16x32_bf16 v[14:17], v[198:201], v[230:233], v[14:17]
	v_mfma_f32_16x16x32_bf16 v[10:13], v[206:209], v[230:233], v[10:13]
	v_mfma_f32_16x16x32_bf16 v[10:13], v[202:205], v[226:229], v[10:13]
	v_mfma_f32_16x16x32_bf16 v[2:5], v[202:205], v[234:237], v[2:5]
	v_mfma_f32_16x16x32_bf16 v[2:5], v[206:209], v[238:241], v[2:5]
	v_mfma_f32_16x16x32_bf16 v[6:9], v[198:201], v[238:241], v[6:9]
	v_mfma_f32_16x16x32_bf16 v[6:9], v[194:197], v[234:237], v[6:9]
	s_barrier
	v_add_u32_e32 v166, 0x18000, v179
	ds_read_b128 v[162:165], v166
	ds_read_b128 v[182:185], v166 offset:1024
	ds_read_b128 v[186:189], v166 offset:2048
	ds_read_b128 v[190:193], v166 offset:3072
	v_add_u32_e32 v166, 0x1c000, v179
	ds_read_b128 v[194:197], v166
	ds_read_b128 v[198:201], v166 offset:1024
	ds_read_b128 v[202:205], v166 offset:2048
	ds_read_b128 v[206:209], v166 offset:3072
	s_add_i32 s29, s29, 0x80000
	s_mov_b32 m0, s43
	ds_read_b128 v[210:213], v180 offset:32768
	ds_read_b128 v[214:217], v180 offset:33792
	ds_read_b128 v[218:221], v180 offset:34816
	ds_read_b128 v[222:225], v180 offset:35840
	ds_read_b128 v[226:229], v180 offset:36864
	ds_read_b128 v[230:233], v180 offset:37888
	ds_read_b128 v[234:237], v180 offset:38912
	ds_read_b128 v[238:241], v180 offset:39936
	buffer_load_dwordx4 v1, s[4:7], s29 offen lds
	s_mov_b32 m0, s44
	s_nop 0
	buffer_load_dwordx4 v175, s[4:7], s29 offen lds
	s_waitcnt vmcnt(8)
	s_waitcnt lgkmcnt(0)
	s_barrier
	s_waitcnt lgkmcnt(7)
	v_mfma_f32_16x16x32_bf16 v[126:129], v[162:165], v[210:213], v[126:129]
	v_mfma_f32_16x16x32_bf16 v[126:129], v[182:185], v[214:217], v[126:129]
	s_waitcnt lgkmcnt(5)
	v_mfma_f32_16x16x32_bf16 v[122:125], v[190:193], v[214:217], v[122:125]
	v_mfma_f32_16x16x32_bf16 v[122:125], v[186:189], v[210:213], v[122:125]
	s_waitcnt lgkmcnt(3)
	v_mfma_f32_16x16x32_bf16 v[114:117], v[186:189], v[218:221], v[114:117]
	v_mfma_f32_16x16x32_bf16 v[114:117], v[190:193], v[222:225], v[114:117]
	s_waitcnt lgkmcnt(1)
	v_mfma_f32_16x16x32_bf16 v[118:121], v[182:185], v[222:225], v[118:121]
	v_mfma_f32_16x16x32_bf16 v[118:121], v[162:165], v[218:221], v[118:121]
	v_mfma_f32_16x16x32_bf16 v[110:113], v[162:165], v[226:229], v[110:113]
	v_mfma_f32_16x16x32_bf16 v[110:113], v[182:185], v[230:233], v[110:113]
	v_mfma_f32_16x16x32_bf16 v[106:109], v[190:193], v[230:233], v[106:109]
	v_mfma_f32_16x16x32_bf16 v[106:109], v[186:189], v[226:229], v[106:109]
	v_mfma_f32_16x16x32_bf16 v[98:101], v[186:189], v[234:237], v[98:101]
	v_mfma_f32_16x16x32_bf16 v[98:101], v[190:193], v[238:241], v[98:101]
	s_waitcnt lgkmcnt(0)
	v_mfma_f32_16x16x32_bf16 v[102:105], v[182:185], v[238:241], v[102:105]
	v_mfma_f32_16x16x32_bf16 v[102:105], v[162:165], v[234:237], v[102:105]
	v_mfma_f32_16x16x32_bf16 v[94:97], v[194:197], v[210:213], v[94:97]
	v_mfma_f32_16x16x32_bf16 v[94:97], v[198:201], v[214:217], v[94:97]
	v_mfma_f32_16x16x32_bf16 v[90:93], v[206:209], v[214:217], v[90:93]
	v_mfma_f32_16x16x32_bf16 v[90:93], v[202:205], v[210:213], v[90:93]
	v_mfma_f32_16x16x32_bf16 v[82:85], v[202:205], v[218:221], v[82:85]
	v_mfma_f32_16x16x32_bf16 v[82:85], v[206:209], v[222:225], v[82:85]
	v_mfma_f32_16x16x32_bf16 v[86:89], v[198:201], v[222:225], v[86:89]
	v_mfma_f32_16x16x32_bf16 v[86:89], v[194:197], v[218:221], v[86:89]
	v_mfma_f32_16x16x32_bf16 v[78:81], v[194:197], v[226:229], v[78:81]
	v_mfma_f32_16x16x32_bf16 v[78:81], v[198:201], v[230:233], v[78:81]
	v_mfma_f32_16x16x32_bf16 v[74:77], v[206:209], v[230:233], v[74:77]
	v_mfma_f32_16x16x32_bf16 v[74:77], v[202:205], v[226:229], v[74:77]
	v_mfma_f32_16x16x32_bf16 v[66:69], v[202:205], v[234:237], v[66:69]
	v_mfma_f32_16x16x32_bf16 v[66:69], v[206:209], v[238:241], v[66:69]
	v_mfma_f32_16x16x32_bf16 v[70:73], v[198:201], v[238:241], v[70:73]
	v_mfma_f32_16x16x32_bf16 v[70:73], v[194:197], v[234:237], v[70:73]
	s_barrier
	s_mov_b32 m0, s49
	ds_read_b128 v[210:213], v180 offset:49152
	ds_read_b128 v[214:217], v180 offset:50176
	ds_read_b128 v[218:221], v180 offset:51200
	ds_read_b128 v[222:225], v180 offset:52224
	ds_read_b128 v[226:229], v180 offset:53248
	ds_read_b128 v[230:233], v180 offset:54272
	ds_read_b128 v[234:237], v180 offset:55296
	ds_read_b128 v[238:241], v180 offset:56320
	buffer_load_dwordx4 v174, s[8:11], s28 offen lds
	s_mov_b32 m0, s50
	s_add_i32 s27, s27, 0x80080
	buffer_load_dwordx4 v176, s[8:11], s28 offen lds
	s_mov_b32 m0, s53
	s_nop 0
	buffer_load_dwordx4 v174, s[8:11], s27 offen lds
	s_mov_b32 m0, s54
	s_nop 0
	buffer_load_dwordx4 v176, s[8:11], s27 offen lds
	s_mov_b32 m0, s51
	s_nop 0
	buffer_load_dwordx4 v1, s[4:7], s26 offen lds
	s_mov_b32 m0, s52
	s_nop 0
	buffer_load_dwordx4 v175, s[4:7], s26 offen lds
	s_waitcnt vmcnt(8)
	s_waitcnt lgkmcnt(0)
	s_barrier
	s_waitcnt lgkmcnt(7)
	v_mfma_f32_16x16x32_bf16 v[62:65], v[162:165], v[210:213], v[62:65]
	v_mfma_f32_16x16x32_bf16 v[62:65], v[182:185], v[214:217], v[62:65]
	s_waitcnt lgkmcnt(5)
	v_mfma_f32_16x16x32_bf16 v[58:61], v[190:193], v[214:217], v[58:61]
	v_mfma_f32_16x16x32_bf16 v[58:61], v[186:189], v[210:213], v[58:61]
	s_waitcnt lgkmcnt(3)
	v_mfma_f32_16x16x32_bf16 v[50:53], v[186:189], v[218:221], v[50:53]
	v_mfma_f32_16x16x32_bf16 v[50:53], v[190:193], v[222:225], v[50:53]
	s_waitcnt lgkmcnt(1)
	v_mfma_f32_16x16x32_bf16 v[54:57], v[182:185], v[222:225], v[54:57]
	v_mfma_f32_16x16x32_bf16 v[54:57], v[162:165], v[218:221], v[54:57]
	v_mfma_f32_16x16x32_bf16 v[46:49], v[162:165], v[226:229], v[46:49]
	v_mfma_f32_16x16x32_bf16 v[46:49], v[182:185], v[230:233], v[46:49]
	v_mfma_f32_16x16x32_bf16 v[42:45], v[190:193], v[230:233], v[42:45]
	v_mfma_f32_16x16x32_bf16 v[42:45], v[186:189], v[226:229], v[42:45]
	v_mfma_f32_16x16x32_bf16 v[34:37], v[186:189], v[234:237], v[34:37]
	v_mfma_f32_16x16x32_bf16 v[34:37], v[190:193], v[238:241], v[34:37]
	s_waitcnt lgkmcnt(0)
	v_mfma_f32_16x16x32_bf16 v[38:41], v[182:185], v[238:241], v[38:41]
	v_mfma_f32_16x16x32_bf16 v[38:41], v[162:165], v[234:237], v[38:41]
	v_mfma_f32_16x16x32_bf16 v[30:33], v[194:197], v[210:213], v[30:33]
	v_mfma_f32_16x16x32_bf16 v[30:33], v[198:201], v[214:217], v[30:33]
	v_mfma_f32_16x16x32_bf16 v[26:29], v[206:209], v[214:217], v[26:29]
	v_mfma_f32_16x16x32_bf16 v[26:29], v[202:205], v[210:213], v[26:29]
	v_mfma_f32_16x16x32_bf16 v[18:21], v[202:205], v[218:221], v[18:21]
	v_mfma_f32_16x16x32_bf16 v[18:21], v[206:209], v[222:225], v[18:21]
	v_mfma_f32_16x16x32_bf16 v[22:25], v[198:201], v[222:225], v[22:25]
	v_mfma_f32_16x16x32_bf16 v[22:25], v[194:197], v[218:221], v[22:25]
	v_mfma_f32_16x16x32_bf16 v[14:17], v[194:197], v[226:229], v[14:17]
	v_mfma_f32_16x16x32_bf16 v[14:17], v[198:201], v[230:233], v[14:17]
	v_mfma_f32_16x16x32_bf16 v[10:13], v[206:209], v[230:233], v[10:13]
	v_mfma_f32_16x16x32_bf16 v[10:13], v[202:205], v[226:229], v[10:13]
	v_mfma_f32_16x16x32_bf16 v[2:5], v[202:205], v[234:237], v[2:5]
	v_mfma_f32_16x16x32_bf16 v[2:5], v[206:209], v[238:241], v[2:5]
	v_mfma_f32_16x16x32_bf16 v[6:9], v[198:201], v[238:241], v[6:9]
	v_mfma_f32_16x16x32_bf16 v[6:9], v[194:197], v[234:237], v[6:9]
	s_barrier
	s_add_i32 s10, s65, 2
	s_addk_i32 s64, 0x100
	s_cmp_gt_u32 s65, 29
	s_cbranch_scc1 .LBB0_910
	s_mov_b32 s65, s10
	s_branch .LBB0_869

.LBB0_1029:
	v_add_u32_e32 v152, 0x10000, v138
	v_add_u32_e32 v168, 0x14000, v138
	ds_read_b128 v[140:143], v152
	ds_read_b128 v[144:147], v152 offset:1024
	ds_read_b128 v[148:151], v152 offset:2048
	ds_read_b128 v[152:155], v152 offset:3072
	ds_read_b128 v[156:159], v168
	ds_read_b128 v[160:163], v168 offset:1024
	ds_read_b128 v[164:167], v168 offset:2048
	ds_read_b128 v[168:171], v168 offset:3072
	s_add_i32 s10, s30, s50
	s_add_i32 s51, s25, s50
	s_add_i32 s11, s10, 0x4000
	s_addk_i32 s51, 0x4000
	s_cmp_eq_u32 s50, 0
	s_cselect_b32 s53, s47, s11
	s_cselect_b32 s52, s48, s51
	s_or_b32 s51, s53, 0x80
	s_add_i32 s10, s10, 0x203f80
	s_mov_b32 m0, s41
	ds_read_b128 v[172:175], v139
	ds_read_b128 v[176:179], v139 offset:1024
	ds_read_b128 v[180:183], v139 offset:2048
	ds_read_b128 v[184:187], v139 offset:3072
	ds_read_b128 v[188:191], v139 offset:4096
	ds_read_b128 v[192:195], v139 offset:5120
	ds_read_b128 v[196:199], v139 offset:6144
	ds_read_b128 v[200:203], v139 offset:7168
	buffer_load_dwordx4 v134, s[4:7], s10 offen lds
	s_mov_b32 m0, s42
	s_nop 0
	buffer_load_dwordx4 v136, s[4:7], s10 offen lds
	s_waitcnt vmcnt(8)
	s_waitcnt lgkmcnt(0)
	s_barrier
	s_waitcnt lgkmcnt(7)
	v_mfma_f32_16x16x32_bf16 v[126:129], v[140:143], v[172:175], v[126:129]
	v_mfma_f32_16x16x32_bf16 v[126:129], v[144:147], v[176:179], v[126:129]
	s_waitcnt lgkmcnt(5)
	v_mfma_f32_16x16x32_bf16 v[122:125], v[152:155], v[176:179], v[122:125]
	v_mfma_f32_16x16x32_bf16 v[122:125], v[148:151], v[172:175], v[122:125]
	s_waitcnt lgkmcnt(3)
	v_mfma_f32_16x16x32_bf16 v[106:109], v[148:151], v[180:183], v[106:109]
	v_mfma_f32_16x16x32_bf16 v[106:109], v[152:155], v[184:187], v[106:109]
	s_waitcnt lgkmcnt(1)
	v_mfma_f32_16x16x32_bf16 v[114:117], v[144:147], v[184:187], v[114:117]
	v_mfma_f32_16x16x32_bf16 v[114:117], v[140:143], v[180:183], v[114:117]
	v_mfma_f32_16x16x32_bf16 v[98:101], v[140:143], v[188:191], v[98:101]
	v_mfma_f32_16x16x32_bf16 v[98:101], v[144:147], v[192:195], v[98:101]
	v_mfma_f32_16x16x32_bf16 v[90:93], v[152:155], v[192:195], v[90:93]
	v_mfma_f32_16x16x32_bf16 v[90:93], v[148:151], v[188:191], v[90:93]
	v_mfma_f32_16x16x32_bf16 v[74:77], v[148:151], v[196:199], v[74:77]
	v_mfma_f32_16x16x32_bf16 v[74:77], v[152:155], v[200:203], v[74:77]
	s_waitcnt lgkmcnt(0)
	v_mfma_f32_16x16x32_bf16 v[82:85], v[144:147], v[200:203], v[82:85]
	v_mfma_f32_16x16x32_bf16 v[82:85], v[140:143], v[196:199], v[82:85]
	v_mfma_f32_16x16x32_bf16 v[118:121], v[156:159], v[172:175], v[118:121]
	v_mfma_f32_16x16x32_bf16 v[118:121], v[160:163], v[176:179], v[118:121]
	v_mfma_f32_16x16x32_bf16 v[110:113], v[168:171], v[176:179], v[110:113]
	v_mfma_f32_16x16x32_bf16 v[110:113], v[164:167], v[172:175], v[110:113]
	v_mfma_f32_16x16x32_bf16 v[94:97], v[164:167], v[180:183], v[94:97]
	v_mfma_f32_16x16x32_bf16 v[94:97], v[168:171], v[184:187], v[94:97]
	v_mfma_f32_16x16x32_bf16 v[102:105], v[160:163], v[184:187], v[102:105]
	v_mfma_f32_16x16x32_bf16 v[102:105], v[156:159], v[180:183], v[102:105]
	v_mfma_f32_16x16x32_bf16 v[86:89], v[156:159], v[188:191], v[86:89]
	v_mfma_f32_16x16x32_bf16 v[86:89], v[160:163], v[192:195], v[86:89]
	v_mfma_f32_16x16x32_bf16 v[78:81], v[168:171], v[192:195], v[78:81]
	v_mfma_f32_16x16x32_bf16 v[78:81], v[164:167], v[188:191], v[78:81]
	v_mfma_f32_16x16x32_bf16 v[66:69], v[164:167], v[196:199], v[66:69]
	v_mfma_f32_16x16x32_bf16 v[66:69], v[168:171], v[200:203], v[66:69]
	v_mfma_f32_16x16x32_bf16 v[70:73], v[160:163], v[200:203], v[70:73]
	v_mfma_f32_16x16x32_bf16 v[70:73], v[156:159], v[196:199], v[70:73]
	s_barrier
	s_mov_b32 m0, s24
	s_mov_b32 s10, s6
	s_mov_b32 s11, s7
	ds_read_b128 v[172:175], v139 offset:16384
	ds_read_b128 v[176:179], v139 offset:17408
	ds_read_b128 v[180:183], v139 offset:18432
	ds_read_b128 v[184:187], v139 offset:19456
	ds_read_b128 v[188:191], v139 offset:20480
	ds_read_b128 v[192:195], v139 offset:21504
	ds_read_b128 v[196:199], v139 offset:22528
	ds_read_b128 v[200:203], v139 offset:23552
	buffer_load_dwordx4 v135, s[8:11], s52 offen lds
	s_mov_b32 m0, s26
	s_add_i32 s54, s52, 0x200000
	buffer_load_dwordx4 v137, s[8:11], s52 offen lds
	s_mov_b32 m0, s27
	s_nop 0
	buffer_load_dwordx4 v135, s[8:11], s54 offen lds
	s_mov_b32 m0, s28
	s_nop 0
	buffer_load_dwordx4 v137, s[8:11], s54 offen lds
	s_mov_b32 m0, s23
	s_nop 0
	buffer_load_dwordx4 v134, s[4:7], s53 offen lds
	s_mov_b32 m0, s29
	s_nop 0
	buffer_load_dwordx4 v136, s[4:7], s53 offen lds
	s_waitcnt vmcnt(8)
	s_waitcnt lgkmcnt(0)
	s_barrier
	s_waitcnt lgkmcnt(7)
	v_mfma_f32_16x16x32_bf16 v[62:65], v[140:143], v[172:175], v[62:65]
	v_mfma_f32_16x16x32_bf16 v[62:65], v[144:147], v[176:179], v[62:65]
	s_waitcnt lgkmcnt(5)
	v_mfma_f32_16x16x32_bf16 v[58:61], v[152:155], v[176:179], v[58:61]
	v_mfma_f32_16x16x32_bf16 v[58:61], v[148:151], v[172:175], v[58:61]
	s_waitcnt lgkmcnt(3)
	v_mfma_f32_16x16x32_bf16 v[42:45], v[148:151], v[180:183], v[42:45]
	v_mfma_f32_16x16x32_bf16 v[42:45], v[152:155], v[184:187], v[42:45]
	s_waitcnt lgkmcnt(1)
	v_mfma_f32_16x16x32_bf16 v[50:53], v[144:147], v[184:187], v[50:53]
	v_mfma_f32_16x16x32_bf16 v[50:53], v[140:143], v[180:183], v[50:53]
	v_mfma_f32_16x16x32_bf16 v[34:37], v[140:143], v[188:191], v[34:37]
	v_mfma_f32_16x16x32_bf16 v[34:37], v[144:147], v[192:195], v[34:37]
	v_mfma_f32_16x16x32_bf16 v[26:29], v[152:155], v[192:195], v[26:29]
	v_mfma_f32_16x16x32_bf16 v[26:29], v[148:151], v[188:191], v[26:29]
	v_mfma_f32_16x16x32_bf16 v[10:13], v[148:151], v[196:199], v[10:13]
	v_mfma_f32_16x16x32_bf16 v[10:13], v[152:155], v[200:203], v[10:13]
	s_waitcnt lgkmcnt(0)
	v_mfma_f32_16x16x32_bf16 v[18:21], v[144:147], v[200:203], v[18:21]
	v_mfma_f32_16x16x32_bf16 v[18:21], v[140:143], v[196:199], v[18:21]
	v_mfma_f32_16x16x32_bf16 v[54:57], v[156:159], v[172:175], v[54:57]
	v_mfma_f32_16x16x32_bf16 v[54:57], v[160:163], v[176:179], v[54:57]
	v_mfma_f32_16x16x32_bf16 v[46:49], v[168:171], v[176:179], v[46:49]
	v_mfma_f32_16x16x32_bf16 v[46:49], v[164:167], v[172:175], v[46:49]
	v_mfma_f32_16x16x32_bf16 v[30:33], v[164:167], v[180:183], v[30:33]
	v_mfma_f32_16x16x32_bf16 v[30:33], v[168:171], v[184:187], v[30:33]
	v_mfma_f32_16x16x32_bf16 v[38:41], v[160:163], v[184:187], v[38:41]
	v_mfma_f32_16x16x32_bf16 v[38:41], v[156:159], v[180:183], v[38:41]
	v_mfma_f32_16x16x32_bf16 v[22:25], v[156:159], v[188:191], v[22:25]
	v_mfma_f32_16x16x32_bf16 v[22:25], v[160:163], v[192:195], v[22:25]
	v_mfma_f32_16x16x32_bf16 v[14:17], v[168:171], v[192:195], v[14:17]
	v_mfma_f32_16x16x32_bf16 v[14:17], v[164:167], v[188:191], v[14:17]
	v_mfma_f32_16x16x32_bf16 v[2:5], v[164:167], v[196:199], v[2:5]
	v_mfma_f32_16x16x32_bf16 v[2:5], v[168:171], v[200:203], v[2:5]
	v_mfma_f32_16x16x32_bf16 v[6:9], v[160:163], v[200:203], v[6:9]
	v_mfma_f32_16x16x32_bf16 v[6:9], v[156:159], v[196:199], v[6:9]
	s_barrier
	v_add_u32_e32 v152, 0x18000, v138
	v_add_u32_e32 v168, 0x1c000, v138
	ds_read_b128 v[140:143], v152
	ds_read_b128 v[144:147], v152 offset:1024
	ds_read_b128 v[148:151], v152 offset:2048
	ds_read_b128 v[152:155], v152 offset:3072
	ds_read_b128 v[156:159], v168
	ds_read_b128 v[160:163], v168 offset:1024
	ds_read_b128 v[164:167], v168 offset:2048
	ds_read_b128 v[168:171], v168 offset:3072
	s_add_i32 s53, s53, 0x200000
	s_mov_b32 m0, s31
	ds_read_b128 v[172:175], v139 offset:32768
	ds_read_b128 v[176:179], v139 offset:33792
	ds_read_b128 v[180:183], v139 offset:34816
	ds_read_b128 v[184:187], v139 offset:35840
	ds_read_b128 v[188:191], v139 offset:36864
	ds_read_b128 v[192:195], v139 offset:37888
	ds_read_b128 v[196:199], v139 offset:38912
	ds_read_b128 v[200:203], v139 offset:39936
	buffer_load_dwordx4 v134, s[4:7], s53 offen lds
	s_mov_b32 m0, s33
	s_nop 0
	buffer_load_dwordx4 v136, s[4:7], s53 offen lds
	s_waitcnt vmcnt(8)
	s_waitcnt lgkmcnt(0)
	s_barrier
	s_waitcnt lgkmcnt(7)
	v_mfma_f32_16x16x32_bf16 v[126:129], v[140:143], v[172:175], v[126:129]
	v_mfma_f32_16x16x32_bf16 v[126:129], v[144:147], v[176:179], v[126:129]
	s_waitcnt lgkmcnt(5)
	v_mfma_f32_16x16x32_bf16 v[122:125], v[152:155], v[176:179], v[122:125]
	v_mfma_f32_16x16x32_bf16 v[122:125], v[148:151], v[172:175], v[122:125]
	s_waitcnt lgkmcnt(3)
	v_mfma_f32_16x16x32_bf16 v[106:109], v[148:151], v[180:183], v[106:109]
	v_mfma_f32_16x16x32_bf16 v[106:109], v[152:155], v[184:187], v[106:109]
	s_waitcnt lgkmcnt(1)
	v_mfma_f32_16x16x32_bf16 v[114:117], v[144:147], v[184:187], v[114:117]
	v_mfma_f32_16x16x32_bf16 v[114:117], v[140:143], v[180:183], v[114:117]
	v_mfma_f32_16x16x32_bf16 v[98:101], v[140:143], v[188:191], v[98:101]
	v_mfma_f32_16x16x32_bf16 v[98:101], v[144:147], v[192:195], v[98:101]
	v_mfma_f32_16x16x32_bf16 v[90:93], v[152:155], v[192:195], v[90:93]
	v_mfma_f32_16x16x32_bf16 v[90:93], v[148:151], v[188:191], v[90:93]
	v_mfma_f32_16x16x32_bf16 v[74:77], v[148:151], v[196:199], v[74:77]
	v_mfma_f32_16x16x32_bf16 v[74:77], v[152:155], v[200:203], v[74:77]
	s_waitcnt lgkmcnt(0)
	v_mfma_f32_16x16x32_bf16 v[82:85], v[144:147], v[200:203], v[82:85]
	v_mfma_f32_16x16x32_bf16 v[82:85], v[140:143], v[196:199], v[82:85]
	v_mfma_f32_16x16x32_bf16 v[118:121], v[156:159], v[172:175], v[118:121]
	v_mfma_f32_16x16x32_bf16 v[118:121], v[160:163], v[176:179], v[118:121]
	v_mfma_f32_16x16x32_bf16 v[110:113], v[168:171], v[176:179], v[110:113]
	v_mfma_f32_16x16x32_bf16 v[110:113], v[164:167], v[172:175], v[110:113]
	v_mfma_f32_16x16x32_bf16 v[94:97], v[164:167], v[180:183], v[94:97]
	v_mfma_f32_16x16x32_bf16 v[94:97], v[168:171], v[184:187], v[94:97]
	v_mfma_f32_16x16x32_bf16 v[102:105], v[160:163], v[184:187], v[102:105]
	v_mfma_f32_16x16x32_bf16 v[102:105], v[156:159], v[180:183], v[102:105]
	v_mfma_f32_16x16x32_bf16 v[86:89], v[156:159], v[188:191], v[86:89]
	v_mfma_f32_16x16x32_bf16 v[86:89], v[160:163], v[192:195], v[86:89]
	v_mfma_f32_16x16x32_bf16 v[78:81], v[168:171], v[192:195], v[78:81]
	v_mfma_f32_16x16x32_bf16 v[78:81], v[164:167], v[188:191], v[78:81]
	v_mfma_f32_16x16x32_bf16 v[66:69], v[164:167], v[196:199], v[66:69]
	v_mfma_f32_16x16x32_bf16 v[66:69], v[168:171], v[200:203], v[66:69]
	v_mfma_f32_16x16x32_bf16 v[70:73], v[160:163], v[200:203], v[70:73]
	v_mfma_f32_16x16x32_bf16 v[70:73], v[156:159], v[196:199], v[70:73]
	s_barrier
	s_mov_b32 m0, s34
	s_or_b32 s53, s52, 0x80
	ds_read_b128 v[172:175], v139 offset:49152
	ds_read_b128 v[176:179], v139 offset:50176
	ds_read_b128 v[180:183], v139 offset:51200
	ds_read_b128 v[184:187], v139 offset:52224
	ds_read_b128 v[188:191], v139 offset:53248
	ds_read_b128 v[192:195], v139 offset:54272
	ds_read_b128 v[196:199], v139 offset:55296
	ds_read_b128 v[200:203], v139 offset:56320
	buffer_load_dwordx4 v135, s[8:11], s53 offen lds
	s_mov_b32 m0, s35
	s_add_i32 s52, s52, 0x200080
	buffer_load_dwordx4 v137, s[8:11], s53 offen lds
	s_mov_b32 m0, s39
	s_nop 0
	buffer_load_dwordx4 v135, s[8:11], s52 offen lds
	s_mov_b32 m0, s40
	s_nop 0
	buffer_load_dwordx4 v137, s[8:11], s52 offen lds
	s_mov_b32 m0, s37
	s_nop 0
	buffer_load_dwordx4 v134, s[4:7], s51 offen lds
	s_mov_b32 m0, s38
	s_nop 0
	buffer_load_dwordx4 v136, s[4:7], s51 offen lds
	s_waitcnt vmcnt(8)
	s_waitcnt lgkmcnt(0)
	s_barrier
	s_waitcnt lgkmcnt(7)
	v_mfma_f32_16x16x32_bf16 v[62:65], v[140:143], v[172:175], v[62:65]
	v_mfma_f32_16x16x32_bf16 v[62:65], v[144:147], v[176:179], v[62:65]
	s_waitcnt lgkmcnt(5)
	v_mfma_f32_16x16x32_bf16 v[58:61], v[152:155], v[176:179], v[58:61]
	v_mfma_f32_16x16x32_bf16 v[58:61], v[148:151], v[172:175], v[58:61]
	s_waitcnt lgkmcnt(3)
	v_mfma_f32_16x16x32_bf16 v[42:45], v[148:151], v[180:183], v[42:45]
	v_mfma_f32_16x16x32_bf16 v[42:45], v[152:155], v[184:187], v[42:45]
	s_waitcnt lgkmcnt(1)
	v_mfma_f32_16x16x32_bf16 v[50:53], v[144:147], v[184:187], v[50:53]
	v_mfma_f32_16x16x32_bf16 v[50:53], v[140:143], v[180:183], v[50:53]
	v_mfma_f32_16x16x32_bf16 v[34:37], v[140:143], v[188:191], v[34:37]
	v_mfma_f32_16x16x32_bf16 v[34:37], v[144:147], v[192:195], v[34:37]
	v_mfma_f32_16x16x32_bf16 v[26:29], v[152:155], v[192:195], v[26:29]
	v_mfma_f32_16x16x32_bf16 v[26:29], v[148:151], v[188:191], v[26:29]
	v_mfma_f32_16x16x32_bf16 v[10:13], v[148:151], v[196:199], v[10:13]
	v_mfma_f32_16x16x32_bf16 v[10:13], v[152:155], v[200:203], v[10:13]
	s_waitcnt lgkmcnt(0)
	v_mfma_f32_16x16x32_bf16 v[18:21], v[144:147], v[200:203], v[18:21]
	v_mfma_f32_16x16x32_bf16 v[18:21], v[140:143], v[196:199], v[18:21]
	v_mfma_f32_16x16x32_bf16 v[54:57], v[156:159], v[172:175], v[54:57]
	v_mfma_f32_16x16x32_bf16 v[54:57], v[160:163], v[176:179], v[54:57]
	v_mfma_f32_16x16x32_bf16 v[46:49], v[168:171], v[176:179], v[46:49]
	v_mfma_f32_16x16x32_bf16 v[46:49], v[164:167], v[172:175], v[46:49]
	v_mfma_f32_16x16x32_bf16 v[30:33], v[164:167], v[180:183], v[30:33]
	v_mfma_f32_16x16x32_bf16 v[30:33], v[168:171], v[184:187], v[30:33]
	v_mfma_f32_16x16x32_bf16 v[38:41], v[160:163], v[184:187], v[38:41]
	v_mfma_f32_16x16x32_bf16 v[38:41], v[156:159], v[180:183], v[38:41]
	v_mfma_f32_16x16x32_bf16 v[22:25], v[156:159], v[188:191], v[22:25]
	v_mfma_f32_16x16x32_bf16 v[22:25], v[160:163], v[192:195], v[22:25]
	v_mfma_f32_16x16x32_bf16 v[14:17], v[168:171], v[192:195], v[14:17]
	v_mfma_f32_16x16x32_bf16 v[14:17], v[164:167], v[188:191], v[14:17]
	v_mfma_f32_16x16x32_bf16 v[2:5], v[164:167], v[196:199], v[2:5]
	v_mfma_f32_16x16x32_bf16 v[2:5], v[168:171], v[200:203], v[2:5]
	v_mfma_f32_16x16x32_bf16 v[6:9], v[160:163], v[200:203], v[6:9]
	v_mfma_f32_16x16x32_bf16 v[6:9], v[156:159], v[196:199], v[6:9]
	s_barrier
	s_add_i32 s49, s49, 2
	s_addk_i32 s50, 0x100
	s_cmpk_gt_u32 s49, 0x7d
	s_cbranch_scc0 .LBB0_1029
	s_andn2_b64 vcc, exec, s[2:3]
	s_cbranch_vccnz .LBB0_1021
	v_mov_b32_e32 v2, 0
	s_mov_b32 s17, s44
	s_mov_b32 s14, s45
	s_mov_b32 s25, s46
	s_mov_b32 s30, s13
	s_mov_b32 s43, s12
	v_mov_b32_e32 v3, v2
	v_mov_b32_e32 v4, v2
	v_mov_b32_e32 v5, v2
	v_mov_b32_e32 v6, v2
	v_mov_b32_e32 v7, v2
	v_mov_b32_e32 v8, v2
	v_mov_b32_e32 v9, v2
	v_mov_b32_e32 v14, v2
	v_mov_b32_e32 v15, v2
	v_mov_b32_e32 v16, v2
	v_mov_b32_e32 v17, v2
	v_mov_b32_e32 v22, v2
	v_mov_b32_e32 v23, v2
	v_mov_b32_e32 v24, v2
	v_mov_b32_e32 v25, v2
	v_mov_b32_e32 v30, v2
	v_mov_b32_e32 v31, v2
	v_mov_b32_e32 v32, v2
	v_mov_b32_e32 v33, v2
	v_mov_b32_e32 v38, v2
	v_mov_b32_e32 v39, v2
	v_mov_b32_e32 v40, v2
	v_mov_b32_e32 v41, v2
	v_mov_b32_e32 v46, v2
	v_mov_b32_e32 v47, v2
	v_mov_b32_e32 v48, v2
	v_mov_b32_e32 v49, v2
	v_mov_b32_e32 v54, v2
	v_mov_b32_e32 v55, v2
	v_mov_b32_e32 v56, v2
	v_mov_b32_e32 v57, v2
	v_mov_b32_e32 v10, v2
	v_mov_b32_e32 v11, v2
	v_mov_b32_e32 v12, v2
	v_mov_b32_e32 v13, v2
	v_mov_b32_e32 v18, v2
	v_mov_b32_e32 v19, v2
	v_mov_b32_e32 v20, v2
	v_mov_b32_e32 v21, v2
	v_mov_b32_e32 v26, v2
	v_mov_b32_e32 v27, v2
	v_mov_b32_e32 v28, v2
	v_mov_b32_e32 v29, v2
	v_mov_b32_e32 v34, v2
	v_mov_b32_e32 v35, v2
	v_mov_b32_e32 v36, v2
	v_mov_b32_e32 v37, v2
	v_mov_b32_e32 v42, v2
	v_mov_b32_e32 v43, v2
	v_mov_b32_e32 v44, v2
	v_mov_b32_e32 v45, v2
	v_mov_b32_e32 v50, v2
	v_mov_b32_e32 v51, v2
	v_mov_b32_e32 v52, v2
	v_mov_b32_e32 v53, v2
	v_mov_b32_e32 v58, v2
	v_mov_b32_e32 v59, v2
	v_mov_b32_e32 v60, v2
	v_mov_b32_e32 v61, v2
	v_mov_b32_e32 v62, v2
	v_mov_b32_e32 v63, v2
	v_mov_b32_e32 v64, v2
	v_mov_b32_e32 v65, v2
	v_mov_b32_e32 v66, v2
	v_mov_b32_e32 v67, v2
	v_mov_b32_e32 v68, v2
	v_mov_b32_e32 v69, v2
	v_mov_b32_e32 v70, v2
	v_mov_b32_e32 v71, v2
	v_mov_b32_e32 v72, v2
	v_mov_b32_e32 v73, v2
	v_mov_b32_e32 v78, v2
	v_mov_b32_e32 v79, v2
	v_mov_b32_e32 v80, v2
	v_mov_b32_e32 v81, v2
	v_mov_b32_e32 v86, v2
	v_mov_b32_e32 v87, v2
	v_mov_b32_e32 v88, v2
	v_mov_b32_e32 v89, v2
	v_mov_b32_e32 v94, v2
	v_mov_b32_e32 v95, v2
	v_mov_b32_e32 v96, v2
	v_mov_b32_e32 v97, v2
	v_mov_b32_e32 v102, v2
	v_mov_b32_e32 v103, v2
	v_mov_b32_e32 v104, v2
	v_mov_b32_e32 v105, v2
	v_mov_b32_e32 v110, v2
	v_mov_b32_e32 v111, v2
	v_mov_b32_e32 v112, v2
	v_mov_b32_e32 v113, v2
	v_mov_b32_e32 v118, v2
	v_mov_b32_e32 v119, v2
	v_mov_b32_e32 v120, v2
	v_mov_b32_e32 v121, v2
	v_mov_b32_e32 v74, v2
	v_mov_b32_e32 v75, v2
	v_mov_b32_e32 v76, v2
	v_mov_b32_e32 v77, v2
	v_mov_b32_e32 v82, v2
	v_mov_b32_e32 v83, v2
	v_mov_b32_e32 v84, v2
	v_mov_b32_e32 v85, v2
	v_mov_b32_e32 v90, v2
	v_mov_b32_e32 v91, v2
	v_mov_b32_e32 v92, v2
	v_mov_b32_e32 v93, v2
	v_mov_b32_e32 v98, v2
	v_mov_b32_e32 v99, v2
	v_mov_b32_e32 v100, v2
	v_mov_b32_e32 v101, v2
	v_mov_b32_e32 v106, v2
	v_mov_b32_e32 v107, v2
	v_mov_b32_e32 v108, v2
	v_mov_b32_e32 v109, v2
	v_mov_b32_e32 v114, v2
	v_mov_b32_e32 v115, v2
	v_mov_b32_e32 v116, v2
	v_mov_b32_e32 v117, v2
	v_mov_b32_e32 v122, v2
	v_mov_b32_e32 v123, v2
	v_mov_b32_e32 v124, v2
	v_mov_b32_e32 v125, v2
	v_mov_b32_e32 v126, v2
	v_mov_b32_e32 v127, v2
	v_mov_b32_e32 v128, v2
	v_mov_b32_e32 v129, v2
	s_branch .LBB0_1021
